# speedup vs baseline: 1.1046x; 1.0197x over previous
_Z11gemm_kernelPKfPKDF16bS0_Pf:
	s_and_b32 s3, s2, 7
	s_ashr_i32 s14, s2, 3
	s_lshl_b32 s12, s3, 6
	s_load_dwordx8 s[4:11], s[0:1], 0x0
	s_add_i32 s12, s12, s14
	s_bfe_u32 s18, s2, 0x10002
	s_lshl_b32 s2, s12, 6
	s_lshl_b32 s13, s18, 14
	s_and_b32 s2, s2, 0x3f00
	v_lshrrev_b32_e32 v52, 6, v0
	v_and_b32_e32 v50, 15, v0
	v_bfe_u32 v51, v0, 4, 2
	v_bfe_u32 v1, v0, 3, 3
	s_or_b32 s2, s2, s13
	v_lshl_or_b32 v102, v52, 2, v51
	v_lshl_or_b32 v104, v52, 3, v1
	v_lshlrev_b32_e32 v1, 4, v50
	s_lshl_b32 s15, s2, 9
	s_waitcnt lgkmcnt(0)
	v_and_b32_e32 v238, 3, v52
	v_lshlrev_b32_e32 v238, 6, v238
	v_lshl_or_b32 v238, v51, 2, v238
	v_lshlrev_b32_e32 v238, 2, v238
	s_and_b32 s24, s12, 3
	s_lshl_b32 s24, s24, 8
	s_lshl_b32 s25, s18, 10
	s_add_u32 s24, s24, s25
	s_lshl_b32 s24, s24, 2
	s_add_u32 s24, s8, s24
	s_addc_u32 s25, s9, 0
	global_load_dwordx4 v[240:243], v238, s[24:25]
	global_load_dwordx4 v[244:247], v238, s[24:25] offset:64
	global_load_dwordx4 v[248:251], v238, s[24:25] offset:128
	global_load_dwordx4 v[252:255], v238, s[24:25] offset:192
	s_mov_b64 s[0:1], s[6:7]
	s_and_b32 s5, s5, 0xffff
	s_mov_b32 s7, 0x20000
	s_brev_b32 s6, -2
	v_lshl_or_b32 v1, v102, 9, v1
	s_or_b32 s2, s15, 0x4000
	s_lshl_b32 s14, s14, 8
	v_lshlrev_b32_e32 v103, 3, v0
	buffer_load_dwordx4 v[54:57], v1, s[4:7], s15 offen sc0 nt
	buffer_load_dwordx4 v[58:61], v1, s[4:7], s2 offen sc0 nt
	s_or_b32 s2, s15, 0x8000
	s_or_b32 s3, s15, 0xc000
	s_lshl_b32 s19, s18, 10
	s_and_b32 s20, s14, 0x300
	v_and_b32_e32 v105, 56, v103
	buffer_load_dwordx4 v[62:65], v1, s[4:7], s2 offen sc0 nt
	buffer_load_dwordx4 v[66:69], v1, s[4:7], s3 offen sc0 nt
	s_or_b32 s2, s15, 0x10000
	s_or_b32 s3, s15, 0x14000
	s_or_b32 s14, s19, s20
	v_lshlrev_b32_e32 v106, 1, v105
	buffer_load_dwordx4 v[70:73], v1, s[4:7], s2 offen sc0 nt
	buffer_load_dwordx4 v[74:77], v1, s[4:7], s3 offen sc0 nt
	s_or_b32 s2, s15, 0x18000
	s_or_b32 s3, s15, 0x1c000
	s_lshl_b32 s14, s14, 11
	buffer_load_dwordx4 v[78:81], v1, s[4:7], s2 offen sc0 nt
	buffer_load_dwordx4 v[82:85], v1, s[4:7], s3 offen sc0 nt
	s_and_b32 s1, s1, 0xffff
	s_mov_b32 s2, s6
	s_mov_b32 s3, s7
	v_lshl_or_b32 v188, v104, 11, v106
	s_or_b32 s16, s14, 0x20000
	buffer_load_dwordx4 v[86:89], v188, s[0:3], s14 offen sc1
	buffer_load_dwordx4 v[90:93], v188, s[0:3], s16 offen sc1
	s_or_b32 s16, s14, 0x40000
	s_or_b32 s17, s14, 0x60000
	buffer_load_dwordx4 v[94:97], v188, s[0:3], s16 offen sc1
	buffer_load_dwordx4 v[98:101], v188, s[0:3], s17 offen sc1
	s_or_b32 s16, s15, 0x100
	s_or_b32 s17, s15, 0x4100
	buffer_load_dwordx4 v[10:13], v1, s[4:7], s16 offen sc0 nt
	buffer_load_dwordx4 v[18:21], v1, s[4:7], s17 offen sc0 nt
	s_or_b32 s16, s15, 0x8100
	s_or_b32 s17, s15, 0xc100
	buffer_load_dwordx4 v[22:25], v1, s[4:7], s16 offen sc0 nt
	buffer_load_dwordx4 v[30:33], v1, s[4:7], s17 offen sc0 nt
	s_or_b32 s16, s15, 0x10100
	s_or_b32 s17, s15, 0x14100
	buffer_load_dwordx4 v[34:37], v1, s[4:7], s16 offen sc0 nt
	buffer_load_dwordx4 v[38:41], v1, s[4:7], s17 offen sc0 nt
	s_or_b32 s16, s15, 0x18100
	s_or_b32 s15, s15, 0x1c100
	buffer_load_dwordx4 v[42:45], v1, s[4:7], s16 offen sc0 nt
	buffer_load_dwordx4 v[46:49], v1, s[4:7], s15 offen sc0 nt
	s_or_b32 s15, s14, 0x80
	s_or_b32 s16, s14, 0x20080
	buffer_load_dwordx4 v[2:5], v188, s[0:3], s15 offen sc1
	buffer_load_dwordx4 v[6:9], v188, s[0:3], s16 offen sc1
	s_or_b32 s15, s14, 0x40080
	s_or_b32 s16, s14, 0x60080
	buffer_load_dwordx4 v[14:17], v188, s[0:3], s15 offen sc1
	buffer_load_dwordx4 v[26:29], v188, s[0:3], s16 offen sc1
	v_lshrrev_b32_e32 v107, 7, v0
	v_bfe_u32 v108, v0, 3, 1
	v_lshlrev_b32_e32 v102, 6, v102
	s_movk_i32 s2, 0x3c0
	v_and_or_b32 v102, v102, s2, v105
	v_lshrrev_b32_e32 v105, 2, v0
	v_and_or_b32 v107, v107, 2, v108
	v_and_b32_e32 v105, 32, v105
	v_lshlrev_b32_e32 v107, 10, v107
	v_bfe_u32 v103, v103, 5, 1
	v_lshlrev_b32_e32 v104, 6, v104
	v_and_b32_e32 v106, 48, v106
	v_bitop3_b32 v189, v102, v107, v105 bitop3:0xde
	v_and_or_b32 v103, v52, 6, v103
	v_and_or_b32 v104, v104, s2, v106
	v_lshrrev_b32_e32 v106, 1, v0
	v_lshlrev_b32_e32 v103, 10, v103
	v_and_b32_e32 v106, 32, v106
	v_bitop3_b32 v190, v104, v103, v106 bitop3:0xde
	v_lshrrev_b32_e32 v53, 8, v0
	s_movk_i32 s15, 0x4000
	s_mov_b32 s16, 0x8000
	s_mov_b32 s17, 0xc000
	s_waitcnt vmcnt(23)
	v_cvt_pk_bf16_f32 v57, v56, v57
	v_cvt_pk_bf16_f32 v56, v54, v55
	s_waitcnt vmcnt(22)
	v_cvt_pk_bf16_f32 v55, v60, v61
	v_cvt_pk_bf16_f32 v54, v58, v59
	ds_write2st64_b64 v189, v[56:57], v[54:55] offset1:8
	s_waitcnt vmcnt(21)
	v_cvt_pk_bf16_f32 v55, v64, v65
	v_cvt_pk_bf16_f32 v54, v62, v63
	s_waitcnt vmcnt(20)
	v_cvt_pk_bf16_f32 v57, v68, v69
	v_cvt_pk_bf16_f32 v56, v66, v67
	ds_write2st64_b64 v189, v[54:55], v[56:57] offset0:16 offset1:24
	s_waitcnt vmcnt(19)
	v_cvt_pk_bf16_f32 v55, v72, v73
	v_cvt_pk_bf16_f32 v54, v70, v71
	s_waitcnt vmcnt(18)
	v_cvt_pk_bf16_f32 v57, v76, v77
	v_cvt_pk_bf16_f32 v56, v74, v75
	ds_write2st64_b64 v189, v[54:55], v[56:57] offset0:32 offset1:40
	s_waitcnt vmcnt(17)
	v_cvt_pk_bf16_f32 v55, v80, v81
	v_cvt_pk_bf16_f32 v54, v78, v79
	s_waitcnt vmcnt(16)
	v_cvt_pk_bf16_f32 v57, v84, v85
	v_cvt_pk_bf16_f32 v56, v82, v83
	ds_write2st64_b64 v189, v[54:55], v[56:57] offset0:48 offset1:56
	s_waitcnt vmcnt(15)
	ds_write_b128 v190, v[86:89] offset:32768
	s_waitcnt vmcnt(14)
	ds_write_b128 v190, v[90:93] offset:40960
	s_waitcnt vmcnt(13)
	ds_write_b128 v190, v[94:97] offset:49152
	s_waitcnt vmcnt(12)
	ds_write_b128 v190, v[98:101] offset:57344
	s_waitcnt lgkmcnt(0)
	s_barrier
	v_cmp_eq_u32_e32 vcc, 1, v53
	s_and_saveexec_b64 s[2:3], vcc
	s_cbranch_execz .LBB1_2
	s_barrier
.LBB1_2:
	s_or_b64 exec, exec, s[2:3]
	v_and_b32_e32 v52, 3, v52
	v_and_b32_e32 v54, 48, v0
	v_lshlrev_b32_e32 v55, 2, v0
	v_lshl_or_b32 v54, v50, 6, v54
	v_and_b32_e32 v55, 32, v55
	v_lshlrev_b32_e32 v56, 14, v53
	v_lshlrev_b32_e32 v57, 13, v52
	v_lshl_or_b32 v52, v52, 6, s20
	v_lshlrev_b32_e32 v51, 2, v51
	s_movk_i32 s2, 0x4c
	v_bitop3_b32 v191, v54, v57, v55 bitop3:0xde
	v_bitop3_b32 v192, v54, v56, v55 bitop3:0xde
	v_or_b32_e32 v54, v52, v51
	v_bitop3_b32 v51, v52, s2, v51 bitop3:0xc8
	v_lshrrev_b32_e32 v52, 6, v52
	s_lshl_b32 s2, s19, 2
	v_and_or_b32 v52, v52, 14, s18
	v_lshlrev_b32_e32 v182, 2, v51
	v_mov_b32_e32 v183, 0
	s_add_u32 s2, s8, s2
	v_lshlrev_b32_e32 v52, 14, v52
	v_lshlrev_b32_e32 v53, 7, v53
	v_lshl_add_u64 v[184:185], s[10:11], 0, v[182:183]
	s_addc_u32 s3, s9, 0
	v_lshlrev_b32_e32 v182, 2, v54
	v_or3_b32 v193, v53, v52, v50
	s_mov_b32 s18, 0
	v_lshl_add_u64 v[186:187], s[2:3], 0, v[182:183]
	s_mov_b32 s2, s6
	s_mov_b32 s3, s7
	s_movk_i32 s8, 0x2000
	s_movk_i32 s9, 0x6000
	s_mov_b32 s10, 0xa000
	s_mov_b32 s11, 0xe000
	s_mov_b32 s19, 0
	s_mov_b32 s20, 0
	s_branch .Lfirst

.LBB1_4:
	v_add_u32_e32 v182, s19, v191
	v_add_u32_e32 v238, s19, v192
	ds_read_b128 v[178:181], v182 offset:32768
	ds_read_b128 v[194:197], v182 offset:34816
	ds_read_b128 v[198:201], v182 offset:36864
	ds_read_b128 v[202:205], v182 offset:38912
	ds_read_b128 v[206:209], v238
	ds_read_b128 v[210:213], v238 offset:2048
	ds_read_b128 v[214:217], v238 offset:4096
	ds_read_b128 v[218:221], v238 offset:6144
	ds_read_b128 v[222:225], v238 offset:8192
	ds_read_b128 v[226:229], v238 offset:10240
	ds_read_b128 v[230:233], v238 offset:12288
	ds_read_b128 v[234:237], v238 offset:14336
	s_min_u32 s21, s20, 29
	s_xor_b32 s19, s19, 0x10000
	v_add_u32_e32 v239, s19, v189
	s_waitcnt vmcnt(11)
	v_cvt_pk_bf16_f32 v13, v12, v13
	v_cvt_pk_bf16_f32 v12, v10, v11
	s_waitcnt vmcnt(10)
	v_cvt_pk_bf16_f32 v11, v20, v21
	v_cvt_pk_bf16_f32 v10, v18, v19
	ds_write2st64_b64 v239, v[12:13], v[10:11] offset1:8
	s_waitcnt vmcnt(9)
	v_cvt_pk_bf16_f32 v11, v24, v25
	v_cvt_pk_bf16_f32 v10, v22, v23
	s_waitcnt vmcnt(8)
	v_cvt_pk_bf16_f32 v13, v32, v33
	v_cvt_pk_bf16_f32 v12, v30, v31
	ds_write2st64_b64 v239, v[10:11], v[12:13] offset0:16 offset1:24
	s_waitcnt vmcnt(7)
	v_cvt_pk_bf16_f32 v11, v36, v37
	v_cvt_pk_bf16_f32 v10, v34, v35
	s_waitcnt vmcnt(6)
	v_cvt_pk_bf16_f32 v13, v40, v41
	v_cvt_pk_bf16_f32 v12, v38, v39
	ds_write2st64_b64 v239, v[10:11], v[12:13] offset0:32 offset1:40
	s_waitcnt vmcnt(5)
	v_cvt_pk_bf16_f32 v11, v44, v45
	v_cvt_pk_bf16_f32 v10, v42, v43
	s_waitcnt vmcnt(4)
	v_cvt_pk_bf16_f32 v13, v48, v49
	v_cvt_pk_bf16_f32 v12, v46, v47
	ds_write2st64_b64 v239, v[10:11], v[12:13] offset0:48 offset1:56
	s_waitcnt lgkmcnt(0)
	s_add_i32 s21, s21, 2
	s_barrier
	s_setprio 1
	s_lshl_b32 s22, s21, 1
	s_and_b32 s22, s22, 0x60
	s_add_i32 s22, s22, s12
	s_lshl_b32 s22, s22, 6
	s_and_b32 s22, s22, 0x3f00
	s_or_b32 s22, s22, s13
	s_lshl_b32 s23, s21, 23
	s_lshl_b32 s22, s22, 9
	s_and_b32 s23, s23, 0x7000000
	s_or_b32 s22, s22, s23
	s_lshl_b32 s23, s21, 8
	s_and_b32 s23, s23, 0x100
	s_or_b32 s22, s22, s23
	s_or_b32 s23, s22, 0x4000
	s_waitcnt lgkmcnt(11)
	v_mfma_f32_16x16x32_bf16 v[174:177], v[178:181], v[206:209], v[174:177]
	v_mfma_f32_16x16x32_bf16 v[170:173], v[194:197], v[206:209], v[170:173]
	v_mfma_f32_16x16x32_bf16 v[158:161], v[198:201], v[206:209], v[158:161]
	buffer_load_dwordx4 v[10:13], v1, s[4:7], s22 offen sc0 nt
	v_mfma_f32_16x16x32_bf16 v[142:145], v[202:205], v[206:209], v[142:145]
	s_waitcnt lgkmcnt(10)
	v_mfma_f32_16x16x32_bf16 v[166:169], v[178:181], v[210:213], v[166:169]
	v_mfma_f32_16x16x32_bf16 v[162:165], v[194:197], v[210:213], v[162:165]
	v_mfma_f32_16x16x32_bf16 v[146:149], v[198:201], v[210:213], v[146:149]
	buffer_load_dwordx4 v[18:21], v1, s[4:7], s23 offen sc0 nt
	s_or_b32 s23, s22, 0x8000
	v_mfma_f32_16x16x32_bf16 v[122:125], v[202:205], v[210:213], v[122:125]
	s_waitcnt lgkmcnt(9)
	v_mfma_f32_16x16x32_bf16 v[154:157], v[178:181], v[214:217], v[154:157]
	v_mfma_f32_16x16x32_bf16 v[150:153], v[194:197], v[214:217], v[150:153]
	v_mfma_f32_16x16x32_bf16 v[130:133], v[198:201], v[214:217], v[130:133]
	buffer_load_dwordx4 v[22:25], v1, s[4:7], s23 offen sc0 nt
	s_or_b32 s23, s22, 0xc000
	v_mfma_f32_16x16x32_bf16 v[106:109], v[202:205], v[214:217], v[106:109]
	s_waitcnt lgkmcnt(8)
	v_mfma_f32_16x16x32_bf16 v[138:141], v[178:181], v[218:221], v[138:141]
	v_mfma_f32_16x16x32_bf16 v[134:137], v[194:197], v[218:221], v[134:137]
	v_mfma_f32_16x16x32_bf16 v[114:117], v[198:201], v[218:221], v[114:117]
	buffer_load_dwordx4 v[30:33], v1, s[4:7], s23 offen sc0 nt
	s_or_b32 s23, s22, 0x10000
	v_mfma_f32_16x16x32_bf16 v[90:93], v[202:205], v[218:221], v[90:93]
	s_waitcnt lgkmcnt(7)
	v_mfma_f32_16x16x32_bf16 v[126:129], v[178:181], v[222:225], v[126:129]
	v_mfma_f32_16x16x32_bf16 v[118:121], v[194:197], v[222:225], v[118:121]
	v_mfma_f32_16x16x32_bf16 v[98:101], v[198:201], v[222:225], v[98:101]
	buffer_load_dwordx4 v[34:37], v1, s[4:7], s23 offen sc0 nt
	s_or_b32 s23, s22, 0x14000
	v_mfma_f32_16x16x32_bf16 v[74:77], v[202:205], v[222:225], v[74:77]
	s_waitcnt lgkmcnt(6)
	v_mfma_f32_16x16x32_bf16 v[110:113], v[178:181], v[226:229], v[110:113]
	v_mfma_f32_16x16x32_bf16 v[102:105], v[194:197], v[226:229], v[102:105]
	v_mfma_f32_16x16x32_bf16 v[82:85], v[198:201], v[226:229], v[82:85]
	buffer_load_dwordx4 v[38:41], v1, s[4:7], s23 offen sc0 nt
	s_or_b32 s23, s22, 0x18000
	s_or_b32 s22, s22, 0x1c000
	v_mfma_f32_16x16x32_bf16 v[62:65], v[202:205], v[226:229], v[62:65]
	s_waitcnt lgkmcnt(5)
	v_mfma_f32_16x16x32_bf16 v[94:97], v[178:181], v[230:233], v[94:97]
	v_mfma_f32_16x16x32_bf16 v[86:89], v[194:197], v[230:233], v[86:89]
	v_mfma_f32_16x16x32_bf16 v[70:73], v[198:201], v[230:233], v[70:73]
	buffer_load_dwordx4 v[42:45], v1, s[4:7], s23 offen sc0 nt
	v_mfma_f32_16x16x32_bf16 v[54:57], v[202:205], v[230:233], v[54:57]
	s_waitcnt lgkmcnt(4)
	v_mfma_f32_16x16x32_bf16 v[78:81], v[178:181], v[234:237], v[78:81]
	v_mfma_f32_16x16x32_bf16 v[66:69], v[194:197], v[234:237], v[66:69]
	v_mfma_f32_16x16x32_bf16 v[58:61], v[198:201], v[234:237], v[58:61]
	buffer_load_dwordx4 v[46:49], v1, s[4:7], s22 offen sc0 nt
	v_mfma_f32_16x16x32_bf16 v[50:53], v[202:205], v[234:237], v[50:53]
	s_setprio 0
	s_waitcnt lgkmcnt(0)
	s_barrier
	ds_read_b128 v[178:181], v182 offset:33792
	ds_read_b128 v[194:197], v182 offset:35840
	ds_read_b128 v[198:201], v182 offset:37888
	ds_read_b128 v[202:205], v182 offset:39936
	ds_read_b128 v[206:209], v238 offset:1024
	ds_read_b128 v[210:213], v238 offset:3072
	ds_read_b128 v[214:217], v238 offset:5120
	ds_read_b128 v[218:221], v238 offset:7168
	ds_read_b128 v[222:225], v238 offset:9216
	ds_read_b128 v[226:229], v238 offset:11264
	ds_read_b128 v[230:233], v238 offset:13312
	ds_read_b128 v[234:237], v238 offset:15360
	v_add_u32_e32 v182, s19, v190
	s_waitcnt vmcnt(11)
	ds_write_b128 v182, v[2:5] offset:32768
	s_waitcnt vmcnt(10)
	ds_write_b128 v182, v[6:9] offset:40960
	s_waitcnt vmcnt(9)
	ds_write_b128 v182, v[14:17] offset:49152
	s_waitcnt vmcnt(8)
	ds_write_b128 v182, v[26:29] offset:57344
	s_waitcnt lgkmcnt(0)
	s_barrier
	s_setprio 1
	s_lshl_b32 s21, s21, 7
	s_and_b32 s21, s21, 0x780
	s_or_b32 s21, s21, s14
	s_or_b32 s22, s21, 0x20000
	s_waitcnt lgkmcnt(11)
	v_mfma_f32_16x16x32_bf16 v[174:177], v[178:181], v[206:209], v[174:177]
	v_mfma_f32_16x16x32_bf16 v[170:173], v[194:197], v[206:209], v[170:173]
	v_mfma_f32_16x16x32_bf16 v[158:161], v[198:201], v[206:209], v[158:161]
	v_mfma_f32_16x16x32_bf16 v[142:145], v[202:205], v[206:209], v[142:145]
	s_waitcnt lgkmcnt(10)
	v_mfma_f32_16x16x32_bf16 v[166:169], v[178:181], v[210:213], v[166:169]
	v_mfma_f32_16x16x32_bf16 v[162:165], v[194:197], v[210:213], v[162:165]
	buffer_load_dwordx4 v[2:5], v188, s[0:3], s21 offen sc1
	v_mfma_f32_16x16x32_bf16 v[146:149], v[198:201], v[210:213], v[146:149]
	v_mfma_f32_16x16x32_bf16 v[122:125], v[202:205], v[210:213], v[122:125]
	s_waitcnt lgkmcnt(9)
	v_mfma_f32_16x16x32_bf16 v[154:157], v[178:181], v[214:217], v[154:157]
	v_mfma_f32_16x16x32_bf16 v[150:153], v[194:197], v[214:217], v[150:153]
	v_mfma_f32_16x16x32_bf16 v[130:133], v[198:201], v[214:217], v[130:133]
	v_mfma_f32_16x16x32_bf16 v[106:109], v[202:205], v[214:217], v[106:109]
	s_waitcnt lgkmcnt(8)
	v_mfma_f32_16x16x32_bf16 v[138:141], v[178:181], v[218:221], v[138:141]
	v_mfma_f32_16x16x32_bf16 v[134:137], v[194:197], v[218:221], v[134:137]
	buffer_load_dwordx4 v[6:9], v188, s[0:3], s22 offen sc1
	s_or_b32 s22, s21, 0x40000
	s_or_b32 s21, s21, 0x60000
	v_mfma_f32_16x16x32_bf16 v[114:117], v[198:201], v[218:221], v[114:117]
	v_mfma_f32_16x16x32_bf16 v[90:93], v[202:205], v[218:221], v[90:93]
	s_waitcnt lgkmcnt(7)
	v_mfma_f32_16x16x32_bf16 v[126:129], v[178:181], v[222:225], v[126:129]
	v_mfma_f32_16x16x32_bf16 v[118:121], v[194:197], v[222:225], v[118:121]
	v_mfma_f32_16x16x32_bf16 v[98:101], v[198:201], v[222:225], v[98:101]
	v_mfma_f32_16x16x32_bf16 v[74:77], v[202:205], v[222:225], v[74:77]
	s_waitcnt lgkmcnt(6)
	v_mfma_f32_16x16x32_bf16 v[110:113], v[178:181], v[226:229], v[110:113]
	v_mfma_f32_16x16x32_bf16 v[102:105], v[194:197], v[226:229], v[102:105]
	buffer_load_dwordx4 v[14:17], v188, s[0:3], s22 offen sc1
	v_mfma_f32_16x16x32_bf16 v[82:85], v[198:201], v[226:229], v[82:85]
	v_mfma_f32_16x16x32_bf16 v[62:65], v[202:205], v[226:229], v[62:65]
	s_waitcnt lgkmcnt(5)
	v_mfma_f32_16x16x32_bf16 v[94:97], v[178:181], v[230:233], v[94:97]
	v_mfma_f32_16x16x32_bf16 v[86:89], v[194:197], v[230:233], v[86:89]
	v_mfma_f32_16x16x32_bf16 v[70:73], v[198:201], v[230:233], v[70:73]
	v_mfma_f32_16x16x32_bf16 v[54:57], v[202:205], v[230:233], v[54:57]
	s_waitcnt lgkmcnt(4)
	v_mfma_f32_16x16x32_bf16 v[78:81], v[178:181], v[234:237], v[78:81]
	v_mfma_f32_16x16x32_bf16 v[66:69], v[194:197], v[234:237], v[66:69]
	buffer_load_dwordx4 v[26:29], v188, s[0:3], s21 offen sc1
	v_mfma_f32_16x16x32_bf16 v[58:61], v[198:201], v[234:237], v[58:61]
	v_mfma_f32_16x16x32_bf16 v[50:53], v[202:205], v[234:237], v[50:53]
	s_setprio 0
	s_and_b32 s21, s20, 15
	s_cmp_lg_u32 s21, 15
	s_cbranch_scc1 .LBB1_3
	s_and_b32 s21, s18, 32
	s_add_i32 s21, s21, s12
	s_lshl_b32 s21, s21, 6
	s_and_b32 s21, s21, 0x3f00
	v_add_lshl_u32 v182, v193, s21, 9
	v_lshl_add_u64 v[206:207], v[184:185], 0, v[182:183]
	v_add_co_u32_e32 v208, vcc, s8, v206
	s_nop 1
	v_addc_co_u32_e32 v209, vcc, 0, v207, vcc
	v_add_co_u32_e32 v210, vcc, s15, v206
	s_nop 1
	v_addc_co_u32_e32 v211, vcc, 0, v207, vcc
	v_add_co_u32_e32 v212, vcc, s9, v206
	s_nop 1
	v_addc_co_u32_e32 v213, vcc, 0, v207, vcc
	v_add_co_u32_e32 v214, vcc, s16, v206
	s_nop 1
	v_addc_co_u32_e32 v215, vcc, 0, v207, vcc
	v_add_co_u32_e32 v216, vcc, s10, v206
	s_nop 1
	v_addc_co_u32_e32 v217, vcc, 0, v207, vcc
	v_add_co_u32_e32 v218, vcc, s17, v206
	s_nop 1
	v_addc_co_u32_e32 v219, vcc, 0, v207, vcc
	v_add_co_u32_e32 v220, vcc, s11, v206
	s_nop 1
	v_addc_co_u32_e32 v221, vcc, 0, v207, vcc
	global_store_dwordx4 v[206:207], v[174:177], off
	global_store_dwordx4 v[206:207], v[170:173], off offset:64
	global_store_dwordx4 v[206:207], v[158:161], off offset:128
	global_store_dwordx4 v[206:207], v[142:145], off offset:192
	global_store_dwordx4 v[208:209], v[166:169], off
	global_store_dwordx4 v[208:209], v[162:165], off offset:64
	global_store_dwordx4 v[208:209], v[146:149], off offset:128
	global_store_dwordx4 v[208:209], v[122:125], off offset:192
	global_store_dwordx4 v[210:211], v[154:157], off
	global_store_dwordx4 v[210:211], v[150:153], off offset:64
	global_store_dwordx4 v[210:211], v[130:133], off offset:128
	global_store_dwordx4 v[210:211], v[106:109], off offset:192
	global_store_dwordx4 v[212:213], v[138:141], off
	global_store_dwordx4 v[212:213], v[134:137], off offset:64
	global_store_dwordx4 v[212:213], v[114:117], off offset:128
	global_store_dwordx4 v[212:213], v[90:93], off offset:192
	global_store_dwordx4 v[214:215], v[126:129], off
	global_store_dwordx4 v[214:215], v[118:121], off offset:64
	global_store_dwordx4 v[214:215], v[98:101], off offset:128
	global_store_dwordx4 v[214:215], v[74:77], off offset:192
	global_store_dwordx4 v[216:217], v[110:113], off
	global_store_dwordx4 v[216:217], v[102:105], off offset:64
	global_store_dwordx4 v[216:217], v[82:85], off offset:128
	global_store_dwordx4 v[216:217], v[62:65], off offset:192
	global_store_dwordx4 v[218:219], v[94:97], off
	global_store_dwordx4 v[218:219], v[86:89], off offset:64
	global_store_dwordx4 v[218:219], v[70:73], off offset:128
	global_store_dwordx4 v[218:219], v[54:57], off offset:192
	global_store_dwordx4 v[220:221], v[78:81], off
	global_store_dwordx4 v[220:221], v[66:69], off offset:64
	global_store_dwordx4 v[220:221], v[58:61], off offset:128
	global_store_dwordx4 v[220:221], v[50:53], off offset:192
.Lpd_tail:
	s_waitcnt lgkmcnt(0)
	s_barrier
	s_add_i32 s20, s20, 1
	s_add_i32 s18, s18, 2
	v_add_u32_e32 v182, s19, v191
	v_add_u32_e32 v238, s19, v192
	ds_read_b128 v[178:181], v182 offset:32768
	ds_read_b128 v[194:197], v182 offset:34816
	ds_read_b128 v[198:201], v182 offset:36864
	ds_read_b128 v[202:205], v182 offset:38912
	ds_read_b128 v[206:209], v238
	ds_read_b128 v[210:213], v238 offset:2048
	ds_read_b128 v[214:217], v238 offset:4096
	ds_read_b128 v[218:221], v238 offset:6144
	ds_read_b128 v[222:225], v238 offset:8192
	ds_read_b128 v[226:229], v238 offset:10240
	ds_read_b128 v[230:233], v238 offset:12288
	ds_read_b128 v[234:237], v238 offset:14336
	s_min_u32 s21, s20, 29
	s_xor_b32 s19, s19, 0x10000
	v_add_u32_e32 v239, s19, v189
	s_waitcnt vmcnt(43)
	v_cvt_pk_bf16_f32 v13, v12, v13
	v_cvt_pk_bf16_f32 v12, v10, v11
	s_waitcnt vmcnt(42)
	v_cvt_pk_bf16_f32 v11, v20, v21
	v_cvt_pk_bf16_f32 v10, v18, v19
	ds_write2st64_b64 v239, v[12:13], v[10:11] offset1:8
	s_waitcnt vmcnt(41)
	v_cvt_pk_bf16_f32 v11, v24, v25
	v_cvt_pk_bf16_f32 v10, v22, v23
	s_waitcnt vmcnt(40)
	v_cvt_pk_bf16_f32 v13, v32, v33
	v_cvt_pk_bf16_f32 v12, v30, v31
	ds_write2st64_b64 v239, v[10:11], v[12:13] offset0:16 offset1:24
	s_waitcnt vmcnt(39)
	v_cvt_pk_bf16_f32 v11, v36, v37
	v_cvt_pk_bf16_f32 v10, v34, v35
	s_waitcnt vmcnt(38)
	v_cvt_pk_bf16_f32 v13, v40, v41
	v_cvt_pk_bf16_f32 v12, v38, v39
	ds_write2st64_b64 v239, v[10:11], v[12:13] offset0:32 offset1:40
	s_waitcnt vmcnt(37)
	v_cvt_pk_bf16_f32 v11, v44, v45
	v_cvt_pk_bf16_f32 v10, v42, v43
	s_waitcnt vmcnt(36)
	v_cvt_pk_bf16_f32 v13, v48, v49
	v_cvt_pk_bf16_f32 v12, v46, v47
	ds_write2st64_b64 v239, v[10:11], v[12:13] offset0:48 offset1:56
	s_waitcnt lgkmcnt(0)
	s_add_i32 s21, s21, 2
	s_barrier
	s_setprio 1
	s_lshl_b32 s22, s21, 1
	s_and_b32 s22, s22, 0x60
	s_add_i32 s22, s22, s12
	s_lshl_b32 s22, s22, 6
	s_and_b32 s22, s22, 0x3f00
	s_or_b32 s22, s22, s13
	s_lshl_b32 s23, s21, 23
	s_lshl_b32 s22, s22, 9
	s_and_b32 s23, s23, 0x7000000
	s_or_b32 s22, s22, s23
	s_lshl_b32 s23, s21, 8
	s_and_b32 s23, s23, 0x100
	s_or_b32 s22, s22, s23
	s_or_b32 s23, s22, 0x4000
	s_waitcnt lgkmcnt(11)
	v_mfma_f32_16x16x32_bf16 v[174:177], v[178:181], v[206:209], v[240:243]
	v_mfma_f32_16x16x32_bf16 v[170:173], v[194:197], v[206:209], v[244:247]
	v_mfma_f32_16x16x32_bf16 v[158:161], v[198:201], v[206:209], v[248:251]
	buffer_load_dwordx4 v[10:13], v1, s[4:7], s22 offen sc0 nt
	v_mfma_f32_16x16x32_bf16 v[142:145], v[202:205], v[206:209], v[252:255]
	s_waitcnt lgkmcnt(10)
	v_mfma_f32_16x16x32_bf16 v[166:169], v[178:181], v[210:213], v[240:243]
	v_mfma_f32_16x16x32_bf16 v[162:165], v[194:197], v[210:213], v[244:247]
	v_mfma_f32_16x16x32_bf16 v[146:149], v[198:201], v[210:213], v[248:251]
	buffer_load_dwordx4 v[18:21], v1, s[4:7], s23 offen sc0 nt
	s_or_b32 s23, s22, 0x8000
	v_mfma_f32_16x16x32_bf16 v[122:125], v[202:205], v[210:213], v[252:255]
	s_waitcnt lgkmcnt(9)
	v_mfma_f32_16x16x32_bf16 v[154:157], v[178:181], v[214:217], v[240:243]
	v_mfma_f32_16x16x32_bf16 v[150:153], v[194:197], v[214:217], v[244:247]
	v_mfma_f32_16x16x32_bf16 v[130:133], v[198:201], v[214:217], v[248:251]
	buffer_load_dwordx4 v[22:25], v1, s[4:7], s23 offen sc0 nt
	s_or_b32 s23, s22, 0xc000
	v_mfma_f32_16x16x32_bf16 v[106:109], v[202:205], v[214:217], v[252:255]
	s_waitcnt lgkmcnt(8)
	v_mfma_f32_16x16x32_bf16 v[138:141], v[178:181], v[218:221], v[240:243]
	v_mfma_f32_16x16x32_bf16 v[134:137], v[194:197], v[218:221], v[244:247]
	v_mfma_f32_16x16x32_bf16 v[114:117], v[198:201], v[218:221], v[248:251]
	buffer_load_dwordx4 v[30:33], v1, s[4:7], s23 offen sc0 nt
	s_or_b32 s23, s22, 0x10000
	v_mfma_f32_16x16x32_bf16 v[90:93], v[202:205], v[218:221], v[252:255]
	s_waitcnt lgkmcnt(7)
	v_mfma_f32_16x16x32_bf16 v[126:129], v[178:181], v[222:225], v[240:243]
	v_mfma_f32_16x16x32_bf16 v[118:121], v[194:197], v[222:225], v[244:247]
	v_mfma_f32_16x16x32_bf16 v[98:101], v[198:201], v[222:225], v[248:251]
	buffer_load_dwordx4 v[34:37], v1, s[4:7], s23 offen sc0 nt
	s_or_b32 s23, s22, 0x14000
	v_mfma_f32_16x16x32_bf16 v[74:77], v[202:205], v[222:225], v[252:255]
	s_waitcnt lgkmcnt(6)
	v_mfma_f32_16x16x32_bf16 v[110:113], v[178:181], v[226:229], v[240:243]
	v_mfma_f32_16x16x32_bf16 v[102:105], v[194:197], v[226:229], v[244:247]
	v_mfma_f32_16x16x32_bf16 v[82:85], v[198:201], v[226:229], v[248:251]
	buffer_load_dwordx4 v[38:41], v1, s[4:7], s23 offen sc0 nt
	s_or_b32 s23, s22, 0x18000
	s_or_b32 s22, s22, 0x1c000
	v_mfma_f32_16x16x32_bf16 v[62:65], v[202:205], v[226:229], v[252:255]
	s_waitcnt lgkmcnt(5)
	v_mfma_f32_16x16x32_bf16 v[94:97], v[178:181], v[230:233], v[240:243]
	v_mfma_f32_16x16x32_bf16 v[86:89], v[194:197], v[230:233], v[244:247]
	v_mfma_f32_16x16x32_bf16 v[70:73], v[198:201], v[230:233], v[248:251]
	buffer_load_dwordx4 v[42:45], v1, s[4:7], s23 offen sc0 nt
	v_mfma_f32_16x16x32_bf16 v[54:57], v[202:205], v[230:233], v[252:255]
	s_waitcnt lgkmcnt(4)
	v_mfma_f32_16x16x32_bf16 v[78:81], v[178:181], v[234:237], v[240:243]
	v_mfma_f32_16x16x32_bf16 v[66:69], v[194:197], v[234:237], v[244:247]
	v_mfma_f32_16x16x32_bf16 v[58:61], v[198:201], v[234:237], v[248:251]
	buffer_load_dwordx4 v[46:49], v1, s[4:7], s22 offen sc0 nt
	v_mfma_f32_16x16x32_bf16 v[50:53], v[202:205], v[234:237], v[252:255]
	s_setprio 0
	s_waitcnt lgkmcnt(0)
	s_barrier
	ds_read_b128 v[178:181], v182 offset:33792
	ds_read_b128 v[194:197], v182 offset:35840
	ds_read_b128 v[198:201], v182 offset:37888
	ds_read_b128 v[202:205], v182 offset:39936
	ds_read_b128 v[206:209], v238 offset:1024
	ds_read_b128 v[210:213], v238 offset:3072
	ds_read_b128 v[214:217], v238 offset:5120
	ds_read_b128 v[218:221], v238 offset:7168
	ds_read_b128 v[222:225], v238 offset:9216
	ds_read_b128 v[226:229], v238 offset:11264
	ds_read_b128 v[230:233], v238 offset:13312
	ds_read_b128 v[234:237], v238 offset:15360
	v_add_u32_e32 v182, s19, v190
	s_waitcnt vmcnt(43)
	ds_write_b128 v182, v[2:5] offset:32768
	s_waitcnt vmcnt(42)
	ds_write_b128 v182, v[6:9] offset:40960
	s_waitcnt vmcnt(41)
	ds_write_b128 v182, v[14:17] offset:49152
	s_waitcnt vmcnt(40)
	ds_write_b128 v182, v[26:29] offset:57344
	s_waitcnt lgkmcnt(0)
	s_barrier
	s_setprio 1
	s_lshl_b32 s21, s21, 7
	s_and_b32 s21, s21, 0x780
	s_or_b32 s21, s21, s14
	s_or_b32 s22, s21, 0x20000
	s_waitcnt lgkmcnt(11)
	v_mfma_f32_16x16x32_bf16 v[174:177], v[178:181], v[206:209], v[174:177]
	v_mfma_f32_16x16x32_bf16 v[170:173], v[194:197], v[206:209], v[170:173]
	v_mfma_f32_16x16x32_bf16 v[158:161], v[198:201], v[206:209], v[158:161]
	v_mfma_f32_16x16x32_bf16 v[142:145], v[202:205], v[206:209], v[142:145]
	s_waitcnt lgkmcnt(10)
	v_mfma_f32_16x16x32_bf16 v[166:169], v[178:181], v[210:213], v[166:169]
	v_mfma_f32_16x16x32_bf16 v[162:165], v[194:197], v[210:213], v[162:165]
	buffer_load_dwordx4 v[2:5], v188, s[0:3], s21 offen sc1
	v_mfma_f32_16x16x32_bf16 v[146:149], v[198:201], v[210:213], v[146:149]
	v_mfma_f32_16x16x32_bf16 v[122:125], v[202:205], v[210:213], v[122:125]
	s_waitcnt lgkmcnt(9)
	v_mfma_f32_16x16x32_bf16 v[154:157], v[178:181], v[214:217], v[154:157]
	v_mfma_f32_16x16x32_bf16 v[150:153], v[194:197], v[214:217], v[150:153]
	v_mfma_f32_16x16x32_bf16 v[130:133], v[198:201], v[214:217], v[130:133]
	v_mfma_f32_16x16x32_bf16 v[106:109], v[202:205], v[214:217], v[106:109]
	s_waitcnt lgkmcnt(8)
	v_mfma_f32_16x16x32_bf16 v[138:141], v[178:181], v[218:221], v[138:141]
	v_mfma_f32_16x16x32_bf16 v[134:137], v[194:197], v[218:221], v[134:137]
	buffer_load_dwordx4 v[6:9], v188, s[0:3], s22 offen sc1
	s_or_b32 s22, s21, 0x40000
	s_or_b32 s21, s21, 0x60000
	v_mfma_f32_16x16x32_bf16 v[114:117], v[198:201], v[218:221], v[114:117]
	v_mfma_f32_16x16x32_bf16 v[90:93], v[202:205], v[218:221], v[90:93]
	s_waitcnt lgkmcnt(7)
	v_mfma_f32_16x16x32_bf16 v[126:129], v[178:181], v[222:225], v[126:129]
	v_mfma_f32_16x16x32_bf16 v[118:121], v[194:197], v[222:225], v[118:121]
	v_mfma_f32_16x16x32_bf16 v[98:101], v[198:201], v[222:225], v[98:101]
	v_mfma_f32_16x16x32_bf16 v[74:77], v[202:205], v[222:225], v[74:77]
	s_waitcnt lgkmcnt(6)
	v_mfma_f32_16x16x32_bf16 v[110:113], v[178:181], v[226:229], v[110:113]
	v_mfma_f32_16x16x32_bf16 v[102:105], v[194:197], v[226:229], v[102:105]
	buffer_load_dwordx4 v[14:17], v188, s[0:3], s22 offen sc1
	v_mfma_f32_16x16x32_bf16 v[82:85], v[198:201], v[226:229], v[82:85]
	v_mfma_f32_16x16x32_bf16 v[62:65], v[202:205], v[226:229], v[62:65]
	s_waitcnt lgkmcnt(5)
	v_mfma_f32_16x16x32_bf16 v[94:97], v[178:181], v[230:233], v[94:97]
	v_mfma_f32_16x16x32_bf16 v[86:89], v[194:197], v[230:233], v[86:89]
	v_mfma_f32_16x16x32_bf16 v[70:73], v[198:201], v[230:233], v[70:73]
	v_mfma_f32_16x16x32_bf16 v[54:57], v[202:205], v[230:233], v[54:57]
	s_waitcnt lgkmcnt(4)
	v_mfma_f32_16x16x32_bf16 v[78:81], v[178:181], v[234:237], v[78:81]
	v_mfma_f32_16x16x32_bf16 v[66:69], v[194:197], v[234:237], v[66:69]
	buffer_load_dwordx4 v[26:29], v188, s[0:3], s21 offen sc1
	v_mfma_f32_16x16x32_bf16 v[58:61], v[198:201], v[234:237], v[58:61]
	v_mfma_f32_16x16x32_bf16 v[50:53], v[202:205], v[234:237], v[50:53]
	s_setprio 0
	s_branch .LBB1_3
.Lt30:
	v_add_u32_e32 v182, s19, v191
	v_add_u32_e32 v238, s19, v192
	ds_read_b128 v[178:181], v182 offset:32768
	ds_read_b128 v[194:197], v182 offset:34816
	ds_read_b128 v[198:201], v182 offset:36864
	ds_read_b128 v[202:205], v182 offset:38912
	ds_read_b128 v[206:209], v238
	ds_read_b128 v[210:213], v238 offset:2048
	ds_read_b128 v[214:217], v238 offset:4096
	ds_read_b128 v[218:221], v238 offset:6144
	ds_read_b128 v[222:225], v238 offset:8192
	ds_read_b128 v[226:229], v238 offset:10240
	ds_read_b128 v[230:233], v238 offset:12288
	ds_read_b128 v[234:237], v238 offset:14336
	s_min_u32 s21, s20, 29
	s_xor_b32 s19, s19, 0x10000
	v_add_u32_e32 v239, s19, v189
	s_waitcnt vmcnt(11)
	v_cvt_pk_bf16_f32 v13, v12, v13
	v_cvt_pk_bf16_f32 v12, v10, v11
	s_waitcnt vmcnt(10)
	v_cvt_pk_bf16_f32 v11, v20, v21
	v_cvt_pk_bf16_f32 v10, v18, v19
	ds_write2st64_b64 v239, v[12:13], v[10:11] offset1:8
	s_waitcnt vmcnt(9)
	v_cvt_pk_bf16_f32 v11, v24, v25
	v_cvt_pk_bf16_f32 v10, v22, v23
	s_waitcnt vmcnt(8)
	v_cvt_pk_bf16_f32 v13, v32, v33
	v_cvt_pk_bf16_f32 v12, v30, v31
	ds_write2st64_b64 v239, v[10:11], v[12:13] offset0:16 offset1:24
	s_waitcnt vmcnt(7)
	v_cvt_pk_bf16_f32 v11, v36, v37
	v_cvt_pk_bf16_f32 v10, v34, v35
	s_waitcnt vmcnt(6)
	v_cvt_pk_bf16_f32 v13, v40, v41
	v_cvt_pk_bf16_f32 v12, v38, v39
	ds_write2st64_b64 v239, v[10:11], v[12:13] offset0:32 offset1:40
	s_waitcnt vmcnt(5)
	v_cvt_pk_bf16_f32 v11, v44, v45
	v_cvt_pk_bf16_f32 v10, v42, v43
	s_waitcnt vmcnt(4)
	v_cvt_pk_bf16_f32 v13, v48, v49
	v_cvt_pk_bf16_f32 v12, v46, v47
	ds_write2st64_b64 v239, v[10:11], v[12:13] offset0:48 offset1:56
	s_waitcnt lgkmcnt(0)
	s_add_i32 s21, s21, 2
	s_barrier
	s_setprio 1
	s_lshl_b32 s22, s21, 1
	s_and_b32 s22, s22, 0x60
	s_add_i32 s22, s22, s12
	s_lshl_b32 s22, s22, 6
	s_and_b32 s22, s22, 0x3f00
	s_or_b32 s22, s22, s13
	s_lshl_b32 s23, s21, 23
	s_lshl_b32 s22, s22, 9
	s_and_b32 s23, s23, 0x7000000
	s_or_b32 s22, s22, s23
	s_lshl_b32 s23, s21, 8
	s_and_b32 s23, s23, 0x100
	s_or_b32 s22, s22, s23
	s_or_b32 s23, s22, 0x4000
	s_waitcnt lgkmcnt(11)
	v_mfma_f32_16x16x32_bf16 v[174:177], v[178:181], v[206:209], v[174:177]
	v_mfma_f32_16x16x32_bf16 v[170:173], v[194:197], v[206:209], v[170:173]
	v_mfma_f32_16x16x32_bf16 v[158:161], v[198:201], v[206:209], v[158:161]
	v_mfma_f32_16x16x32_bf16 v[142:145], v[202:205], v[206:209], v[142:145]
	s_waitcnt lgkmcnt(10)
	v_mfma_f32_16x16x32_bf16 v[166:169], v[178:181], v[210:213], v[166:169]
	v_mfma_f32_16x16x32_bf16 v[162:165], v[194:197], v[210:213], v[162:165]
	v_mfma_f32_16x16x32_bf16 v[146:149], v[198:201], v[210:213], v[146:149]
	s_or_b32 s23, s22, 0x8000
	v_mfma_f32_16x16x32_bf16 v[122:125], v[202:205], v[210:213], v[122:125]
	s_waitcnt lgkmcnt(9)
	v_mfma_f32_16x16x32_bf16 v[154:157], v[178:181], v[214:217], v[154:157]
	v_mfma_f32_16x16x32_bf16 v[150:153], v[194:197], v[214:217], v[150:153]
	v_mfma_f32_16x16x32_bf16 v[130:133], v[198:201], v[214:217], v[130:133]
	s_or_b32 s23, s22, 0xc000
	v_mfma_f32_16x16x32_bf16 v[106:109], v[202:205], v[214:217], v[106:109]
	s_waitcnt lgkmcnt(8)
	v_mfma_f32_16x16x32_bf16 v[138:141], v[178:181], v[218:221], v[138:141]
	v_mfma_f32_16x16x32_bf16 v[134:137], v[194:197], v[218:221], v[134:137]
	v_mfma_f32_16x16x32_bf16 v[114:117], v[198:201], v[218:221], v[114:117]
	s_or_b32 s23, s22, 0x10000
	v_mfma_f32_16x16x32_bf16 v[90:93], v[202:205], v[218:221], v[90:93]
	s_waitcnt lgkmcnt(7)
	v_mfma_f32_16x16x32_bf16 v[126:129], v[178:181], v[222:225], v[126:129]
	v_mfma_f32_16x16x32_bf16 v[118:121], v[194:197], v[222:225], v[118:121]
	v_mfma_f32_16x16x32_bf16 v[98:101], v[198:201], v[222:225], v[98:101]
	s_or_b32 s23, s22, 0x14000
	v_mfma_f32_16x16x32_bf16 v[74:77], v[202:205], v[222:225], v[74:77]
	s_waitcnt lgkmcnt(6)
	v_mfma_f32_16x16x32_bf16 v[110:113], v[178:181], v[226:229], v[110:113]
	v_mfma_f32_16x16x32_bf16 v[102:105], v[194:197], v[226:229], v[102:105]
	v_mfma_f32_16x16x32_bf16 v[82:85], v[198:201], v[226:229], v[82:85]
	s_or_b32 s23, s22, 0x18000
	s_or_b32 s22, s22, 0x1c000
	v_mfma_f32_16x16x32_bf16 v[62:65], v[202:205], v[226:229], v[62:65]
	s_waitcnt lgkmcnt(5)
	v_mfma_f32_16x16x32_bf16 v[94:97], v[178:181], v[230:233], v[94:97]
	v_mfma_f32_16x16x32_bf16 v[86:89], v[194:197], v[230:233], v[86:89]
	v_mfma_f32_16x16x32_bf16 v[70:73], v[198:201], v[230:233], v[70:73]
	v_mfma_f32_16x16x32_bf16 v[54:57], v[202:205], v[230:233], v[54:57]
	s_waitcnt lgkmcnt(4)
	v_mfma_f32_16x16x32_bf16 v[78:81], v[178:181], v[234:237], v[78:81]
	v_mfma_f32_16x16x32_bf16 v[66:69], v[194:197], v[234:237], v[66:69]
	v_mfma_f32_16x16x32_bf16 v[58:61], v[198:201], v[234:237], v[58:61]
	v_mfma_f32_16x16x32_bf16 v[50:53], v[202:205], v[234:237], v[50:53]
	s_setprio 0
	s_waitcnt lgkmcnt(0)
	s_barrier
	ds_read_b128 v[178:181], v182 offset:33792
	ds_read_b128 v[194:197], v182 offset:35840
	ds_read_b128 v[198:201], v182 offset:37888
	ds_read_b128 v[202:205], v182 offset:39936
	ds_read_b128 v[206:209], v238 offset:1024
	ds_read_b128 v[210:213], v238 offset:3072
	ds_read_b128 v[214:217], v238 offset:5120
	ds_read_b128 v[218:221], v238 offset:7168
	ds_read_b128 v[222:225], v238 offset:9216
	ds_read_b128 v[226:229], v238 offset:11264
	ds_read_b128 v[230:233], v238 offset:13312
	ds_read_b128 v[234:237], v238 offset:15360
	v_add_u32_e32 v182, s19, v190
	s_waitcnt vmcnt(3)
	ds_write_b128 v182, v[2:5] offset:32768
	s_waitcnt vmcnt(2)
	ds_write_b128 v182, v[6:9] offset:40960
	s_waitcnt vmcnt(1)
	ds_write_b128 v182, v[14:17] offset:49152
	s_waitcnt vmcnt(0)
	ds_write_b128 v182, v[26:29] offset:57344
	s_waitcnt lgkmcnt(0)
	s_barrier
	s_setprio 1
	s_lshl_b32 s21, s21, 7
	s_and_b32 s21, s21, 0x780
	s_or_b32 s21, s21, s14
	s_or_b32 s22, s21, 0x20000
	s_waitcnt lgkmcnt(11)
	v_mfma_f32_16x16x32_bf16 v[174:177], v[178:181], v[206:209], v[174:177]
	v_mfma_f32_16x16x32_bf16 v[170:173], v[194:197], v[206:209], v[170:173]
	v_mfma_f32_16x16x32_bf16 v[158:161], v[198:201], v[206:209], v[158:161]
	v_mfma_f32_16x16x32_bf16 v[142:145], v[202:205], v[206:209], v[142:145]
	s_waitcnt lgkmcnt(10)
	v_mfma_f32_16x16x32_bf16 v[166:169], v[178:181], v[210:213], v[166:169]
	v_mfma_f32_16x16x32_bf16 v[162:165], v[194:197], v[210:213], v[162:165]
	v_mfma_f32_16x16x32_bf16 v[146:149], v[198:201], v[210:213], v[146:149]
	v_mfma_f32_16x16x32_bf16 v[122:125], v[202:205], v[210:213], v[122:125]
	s_waitcnt lgkmcnt(9)
	v_mfma_f32_16x16x32_bf16 v[154:157], v[178:181], v[214:217], v[154:157]
	v_mfma_f32_16x16x32_bf16 v[150:153], v[194:197], v[214:217], v[150:153]
	v_mfma_f32_16x16x32_bf16 v[130:133], v[198:201], v[214:217], v[130:133]
	v_mfma_f32_16x16x32_bf16 v[106:109], v[202:205], v[214:217], v[106:109]
	s_waitcnt lgkmcnt(8)
	v_mfma_f32_16x16x32_bf16 v[138:141], v[178:181], v[218:221], v[138:141]
	v_mfma_f32_16x16x32_bf16 v[134:137], v[194:197], v[218:221], v[134:137]
	s_or_b32 s22, s21, 0x40000
	s_or_b32 s21, s21, 0x60000
	v_mfma_f32_16x16x32_bf16 v[114:117], v[198:201], v[218:221], v[114:117]
	v_mfma_f32_16x16x32_bf16 v[90:93], v[202:205], v[218:221], v[90:93]
	s_waitcnt lgkmcnt(7)
	v_mfma_f32_16x16x32_bf16 v[126:129], v[178:181], v[222:225], v[126:129]
	v_mfma_f32_16x16x32_bf16 v[118:121], v[194:197], v[222:225], v[118:121]
	v_mfma_f32_16x16x32_bf16 v[98:101], v[198:201], v[222:225], v[98:101]
	v_mfma_f32_16x16x32_bf16 v[74:77], v[202:205], v[222:225], v[74:77]
	s_waitcnt lgkmcnt(6)
	v_mfma_f32_16x16x32_bf16 v[110:113], v[178:181], v[226:229], v[110:113]
	v_mfma_f32_16x16x32_bf16 v[102:105], v[194:197], v[226:229], v[102:105]
	v_mfma_f32_16x16x32_bf16 v[82:85], v[198:201], v[226:229], v[82:85]
	v_mfma_f32_16x16x32_bf16 v[62:65], v[202:205], v[226:229], v[62:65]
	s_waitcnt lgkmcnt(5)
	v_mfma_f32_16x16x32_bf16 v[94:97], v[178:181], v[230:233], v[94:97]
	v_mfma_f32_16x16x32_bf16 v[86:89], v[194:197], v[230:233], v[86:89]
	v_mfma_f32_16x16x32_bf16 v[70:73], v[198:201], v[230:233], v[70:73]
	v_mfma_f32_16x16x32_bf16 v[54:57], v[202:205], v[230:233], v[54:57]
	s_waitcnt lgkmcnt(4)
	v_mfma_f32_16x16x32_bf16 v[78:81], v[178:181], v[234:237], v[78:81]
	v_mfma_f32_16x16x32_bf16 v[66:69], v[194:197], v[234:237], v[66:69]
	v_mfma_f32_16x16x32_bf16 v[58:61], v[198:201], v[234:237], v[58:61]
	v_mfma_f32_16x16x32_bf16 v[50:53], v[202:205], v[234:237], v[50:53]
	s_setprio 0
	s_waitcnt lgkmcnt(0)
	s_barrier
	s_add_i32 s20, s20, 1
	s_add_i32 s18, s18, 2
	v_add_u32_e32 v182, s19, v191
	v_add_u32_e32 v238, s19, v192
	ds_read_b128 v[178:181], v182 offset:32768
	ds_read_b128 v[194:197], v182 offset:34816
	ds_read_b128 v[198:201], v182 offset:36864
	ds_read_b128 v[202:205], v182 offset:38912
	ds_read_b128 v[206:209], v238
	ds_read_b128 v[210:213], v238 offset:2048
	ds_read_b128 v[214:217], v238 offset:4096
	ds_read_b128 v[218:221], v238 offset:6144
	ds_read_b128 v[222:225], v238 offset:8192
	ds_read_b128 v[226:229], v238 offset:10240
	ds_read_b128 v[230:233], v238 offset:12288
	ds_read_b128 v[234:237], v238 offset:14336
	s_min_u32 s21, s20, 29
	s_xor_b32 s19, s19, 0x10000
	v_add_u32_e32 v239, s19, v189
	s_waitcnt lgkmcnt(0)
	s_add_i32 s21, s21, 2
	s_barrier
	s_setprio 1
	s_lshl_b32 s22, s21, 1
	s_and_b32 s22, s22, 0x60
	s_add_i32 s22, s22, s12
	s_lshl_b32 s22, s22, 6
	s_and_b32 s22, s22, 0x3f00
	s_or_b32 s22, s22, s13
	s_lshl_b32 s23, s21, 23
	s_lshl_b32 s22, s22, 9
	s_and_b32 s23, s23, 0x7000000
	s_or_b32 s22, s22, s23
	s_lshl_b32 s23, s21, 8
	s_and_b32 s23, s23, 0x100
	s_or_b32 s22, s22, s23
	s_or_b32 s23, s22, 0x4000
	s_waitcnt lgkmcnt(11)
	v_mfma_f32_16x16x32_bf16 v[174:177], v[178:181], v[206:209], v[174:177]
	v_mfma_f32_16x16x32_bf16 v[170:173], v[194:197], v[206:209], v[170:173]
	v_mfma_f32_16x16x32_bf16 v[158:161], v[198:201], v[206:209], v[158:161]
	v_mfma_f32_16x16x32_bf16 v[142:145], v[202:205], v[206:209], v[142:145]
	s_waitcnt lgkmcnt(10)
	v_mfma_f32_16x16x32_bf16 v[166:169], v[178:181], v[210:213], v[166:169]
	v_mfma_f32_16x16x32_bf16 v[162:165], v[194:197], v[210:213], v[162:165]
	v_mfma_f32_16x16x32_bf16 v[146:149], v[198:201], v[210:213], v[146:149]
	s_or_b32 s23, s22, 0x8000
	v_mfma_f32_16x16x32_bf16 v[122:125], v[202:205], v[210:213], v[122:125]
	s_waitcnt lgkmcnt(9)
	v_mfma_f32_16x16x32_bf16 v[154:157], v[178:181], v[214:217], v[154:157]
	v_mfma_f32_16x16x32_bf16 v[150:153], v[194:197], v[214:217], v[150:153]
	v_mfma_f32_16x16x32_bf16 v[130:133], v[198:201], v[214:217], v[130:133]
	s_or_b32 s23, s22, 0xc000
	v_mfma_f32_16x16x32_bf16 v[106:109], v[202:205], v[214:217], v[106:109]
	s_waitcnt lgkmcnt(8)
	v_mfma_f32_16x16x32_bf16 v[138:141], v[178:181], v[218:221], v[138:141]
	v_mfma_f32_16x16x32_bf16 v[134:137], v[194:197], v[218:221], v[134:137]
	v_mfma_f32_16x16x32_bf16 v[114:117], v[198:201], v[218:221], v[114:117]
	s_or_b32 s23, s22, 0x10000
	v_mfma_f32_16x16x32_bf16 v[90:93], v[202:205], v[218:221], v[90:93]
	s_waitcnt lgkmcnt(7)
	v_mfma_f32_16x16x32_bf16 v[126:129], v[178:181], v[222:225], v[126:129]
	v_mfma_f32_16x16x32_bf16 v[118:121], v[194:197], v[222:225], v[118:121]
	v_mfma_f32_16x16x32_bf16 v[98:101], v[198:201], v[222:225], v[98:101]
	s_or_b32 s23, s22, 0x14000
	v_mfma_f32_16x16x32_bf16 v[74:77], v[202:205], v[222:225], v[74:77]
	s_waitcnt lgkmcnt(6)
	v_mfma_f32_16x16x32_bf16 v[110:113], v[178:181], v[226:229], v[110:113]
	v_mfma_f32_16x16x32_bf16 v[102:105], v[194:197], v[226:229], v[102:105]
	v_mfma_f32_16x16x32_bf16 v[82:85], v[198:201], v[226:229], v[82:85]
	s_or_b32 s23, s22, 0x18000
	s_or_b32 s22, s22, 0x1c000
	v_mfma_f32_16x16x32_bf16 v[62:65], v[202:205], v[226:229], v[62:65]
	s_waitcnt lgkmcnt(5)
	v_mfma_f32_16x16x32_bf16 v[94:97], v[178:181], v[230:233], v[94:97]
	v_mfma_f32_16x16x32_bf16 v[86:89], v[194:197], v[230:233], v[86:89]
	v_mfma_f32_16x16x32_bf16 v[70:73], v[198:201], v[230:233], v[70:73]
	v_mfma_f32_16x16x32_bf16 v[54:57], v[202:205], v[230:233], v[54:57]
	s_waitcnt lgkmcnt(4)
	v_mfma_f32_16x16x32_bf16 v[78:81], v[178:181], v[234:237], v[78:81]
	v_mfma_f32_16x16x32_bf16 v[66:69], v[194:197], v[234:237], v[66:69]
	v_mfma_f32_16x16x32_bf16 v[58:61], v[198:201], v[234:237], v[58:61]
	v_mfma_f32_16x16x32_bf16 v[50:53], v[202:205], v[234:237], v[50:53]
	s_setprio 0
	s_waitcnt lgkmcnt(0)
	s_barrier
	ds_read_b128 v[178:181], v182 offset:33792
	ds_read_b128 v[194:197], v182 offset:35840
	ds_read_b128 v[198:201], v182 offset:37888
	ds_read_b128 v[202:205], v182 offset:39936
	ds_read_b128 v[206:209], v238 offset:1024
	ds_read_b128 v[210:213], v238 offset:3072
	ds_read_b128 v[214:217], v238 offset:5120
	ds_read_b128 v[218:221], v238 offset:7168
	ds_read_b128 v[222:225], v238 offset:9216
	ds_read_b128 v[226:229], v238 offset:11264
	ds_read_b128 v[230:233], v238 offset:13312
	ds_read_b128 v[234:237], v238 offset:15360
	s_waitcnt lgkmcnt(0)
	s_barrier
	s_setprio 1
	s_lshl_b32 s21, s21, 7
	s_and_b32 s21, s21, 0x780
	s_or_b32 s21, s21, s14
	s_or_b32 s22, s21, 0x20000
	s_waitcnt lgkmcnt(11)
	v_mfma_f32_16x16x32_bf16 v[174:177], v[178:181], v[206:209], v[174:177]
	v_mfma_f32_16x16x32_bf16 v[170:173], v[194:197], v[206:209], v[170:173]
	v_mfma_f32_16x16x32_bf16 v[158:161], v[198:201], v[206:209], v[158:161]
	v_mfma_f32_16x16x32_bf16 v[142:145], v[202:205], v[206:209], v[142:145]
	s_waitcnt lgkmcnt(10)
	v_mfma_f32_16x16x32_bf16 v[166:169], v[178:181], v[210:213], v[166:169]
	v_mfma_f32_16x16x32_bf16 v[162:165], v[194:197], v[210:213], v[162:165]
	v_mfma_f32_16x16x32_bf16 v[146:149], v[198:201], v[210:213], v[146:149]
	v_mfma_f32_16x16x32_bf16 v[122:125], v[202:205], v[210:213], v[122:125]
	s_waitcnt lgkmcnt(9)
	v_mfma_f32_16x16x32_bf16 v[154:157], v[178:181], v[214:217], v[154:157]
	v_mfma_f32_16x16x32_bf16 v[150:153], v[194:197], v[214:217], v[150:153]
	v_mfma_f32_16x16x32_bf16 v[130:133], v[198:201], v[214:217], v[130:133]
	v_mfma_f32_16x16x32_bf16 v[106:109], v[202:205], v[214:217], v[106:109]
	s_waitcnt lgkmcnt(8)
	v_mfma_f32_16x16x32_bf16 v[138:141], v[178:181], v[218:221], v[138:141]
	v_mfma_f32_16x16x32_bf16 v[134:137], v[194:197], v[218:221], v[134:137]
	s_or_b32 s22, s21, 0x40000
	s_or_b32 s21, s21, 0x60000
	v_mfma_f32_16x16x32_bf16 v[114:117], v[198:201], v[218:221], v[114:117]
	v_mfma_f32_16x16x32_bf16 v[90:93], v[202:205], v[218:221], v[90:93]
	s_waitcnt lgkmcnt(7)
	v_mfma_f32_16x16x32_bf16 v[126:129], v[178:181], v[222:225], v[126:129]
	v_mfma_f32_16x16x32_bf16 v[118:121], v[194:197], v[222:225], v[118:121]
	v_mfma_f32_16x16x32_bf16 v[98:101], v[198:201], v[222:225], v[98:101]
	v_mfma_f32_16x16x32_bf16 v[74:77], v[202:205], v[222:225], v[74:77]
	s_waitcnt lgkmcnt(6)
	v_mfma_f32_16x16x32_bf16 v[110:113], v[178:181], v[226:229], v[110:113]
	v_mfma_f32_16x16x32_bf16 v[102:105], v[194:197], v[226:229], v[102:105]
	v_mfma_f32_16x16x32_bf16 v[82:85], v[198:201], v[226:229], v[82:85]
	v_mfma_f32_16x16x32_bf16 v[62:65], v[202:205], v[226:229], v[62:65]
	s_waitcnt lgkmcnt(5)
	v_mfma_f32_16x16x32_bf16 v[94:97], v[178:181], v[230:233], v[94:97]
	v_mfma_f32_16x16x32_bf16 v[86:89], v[194:197], v[230:233], v[86:89]
	v_mfma_f32_16x16x32_bf16 v[70:73], v[198:201], v[230:233], v[70:73]
	v_mfma_f32_16x16x32_bf16 v[54:57], v[202:205], v[230:233], v[54:57]
	s_waitcnt lgkmcnt(4)
	v_mfma_f32_16x16x32_bf16 v[78:81], v[178:181], v[234:237], v[78:81]
	v_mfma_f32_16x16x32_bf16 v[66:69], v[194:197], v[234:237], v[66:69]
	v_mfma_f32_16x16x32_bf16 v[58:61], v[198:201], v[234:237], v[58:61]
	v_mfma_f32_16x16x32_bf16 v[50:53], v[202:205], v[234:237], v[50:53]
	s_setprio 0
	s_and_b32 s21, s18, 32
	s_add_i32 s21, s21, s12
	s_lshl_b32 s21, s21, 6
	s_and_b32 s21, s21, 0x3f00
	v_add_lshl_u32 v182, v193, s21, 9
	v_lshl_add_u64 v[206:207], v[184:185], 0, v[182:183]
	v_add_co_u32_e32 v208, vcc, s8, v206
	s_nop 1
	v_addc_co_u32_e32 v209, vcc, 0, v207, vcc
	v_add_co_u32_e32 v210, vcc, s15, v206
	s_nop 1
	v_addc_co_u32_e32 v211, vcc, 0, v207, vcc
	v_add_co_u32_e32 v212, vcc, s9, v206
	s_nop 1
	v_addc_co_u32_e32 v213, vcc, 0, v207, vcc
	v_add_co_u32_e32 v214, vcc, s16, v206
	s_nop 1
	v_addc_co_u32_e32 v215, vcc, 0, v207, vcc
	v_add_co_u32_e32 v216, vcc, s10, v206
	s_nop 1
	v_addc_co_u32_e32 v217, vcc, 0, v207, vcc
	v_add_co_u32_e32 v218, vcc, s17, v206
	s_nop 1
	v_addc_co_u32_e32 v219, vcc, 0, v207, vcc
	v_add_co_u32_e32 v220, vcc, s11, v206
	s_nop 1
	v_addc_co_u32_e32 v221, vcc, 0, v207, vcc
	global_store_dwordx4 v[206:207], v[174:177], off
	global_store_dwordx4 v[206:207], v[170:173], off offset:64
	global_store_dwordx4 v[206:207], v[158:161], off offset:128
	global_store_dwordx4 v[206:207], v[142:145], off offset:192
	global_store_dwordx4 v[208:209], v[166:169], off
	global_store_dwordx4 v[208:209], v[162:165], off offset:64
	global_store_dwordx4 v[208:209], v[146:149], off offset:128
	global_store_dwordx4 v[208:209], v[122:125], off offset:192
	global_store_dwordx4 v[210:211], v[154:157], off
	global_store_dwordx4 v[210:211], v[150:153], off offset:64
	global_store_dwordx4 v[210:211], v[130:133], off offset:128
	global_store_dwordx4 v[210:211], v[106:109], off offset:192
	global_store_dwordx4 v[212:213], v[138:141], off
	global_store_dwordx4 v[212:213], v[134:137], off offset:64
	global_store_dwordx4 v[212:213], v[114:117], off offset:128
	global_store_dwordx4 v[212:213], v[90:93], off offset:192
	global_store_dwordx4 v[214:215], v[126:129], off
	global_store_dwordx4 v[214:215], v[118:121], off offset:64
	global_store_dwordx4 v[214:215], v[98:101], off offset:128
	global_store_dwordx4 v[214:215], v[74:77], off offset:192
	global_store_dwordx4 v[216:217], v[110:113], off
	global_store_dwordx4 v[216:217], v[102:105], off offset:64
	global_store_dwordx4 v[216:217], v[82:85], off offset:128
	global_store_dwordx4 v[216:217], v[62:65], off offset:192
	global_store_dwordx4 v[218:219], v[94:97], off
	global_store_dwordx4 v[218:219], v[86:89], off offset:64
	global_store_dwordx4 v[218:219], v[70:73], off offset:128
	global_store_dwordx4 v[218:219], v[54:57], off offset:192
	global_store_dwordx4 v[220:221], v[78:81], off
	global_store_dwordx4 v[220:221], v[66:69], off offset:64
	global_store_dwordx4 v[220:221], v[58:61], off offset:128
	global_store_dwordx4 v[220:221], v[50:53], off offset:192
	s_waitcnt lgkmcnt(0)
	s_barrier
	s_branch .LBB1_6
.Lfirst:
	v_add_u32_e32 v182, s19, v191
	v_add_u32_e32 v238, s19, v192
	ds_read_b128 v[178:181], v182 offset:32768
	ds_read_b128 v[194:197], v182 offset:34816
	ds_read_b128 v[198:201], v182 offset:36864
	ds_read_b128 v[202:205], v182 offset:38912
	ds_read_b128 v[206:209], v238
	ds_read_b128 v[210:213], v238 offset:2048
	ds_read_b128 v[214:217], v238 offset:4096
	ds_read_b128 v[218:221], v238 offset:6144
	ds_read_b128 v[222:225], v238 offset:8192
	ds_read_b128 v[226:229], v238 offset:10240
	ds_read_b128 v[230:233], v238 offset:12288
	ds_read_b128 v[234:237], v238 offset:14336
	s_min_u32 s21, s20, 29
	s_xor_b32 s19, s19, 0x10000
	v_add_u32_e32 v239, s19, v189
	s_waitcnt vmcnt(11)
	v_cvt_pk_bf16_f32 v13, v12, v13
	v_cvt_pk_bf16_f32 v12, v10, v11
	s_waitcnt vmcnt(10)
	v_cvt_pk_bf16_f32 v11, v20, v21
	v_cvt_pk_bf16_f32 v10, v18, v19
	ds_write2st64_b64 v239, v[12:13], v[10:11] offset1:8
	s_waitcnt vmcnt(9)
	v_cvt_pk_bf16_f32 v11, v24, v25
	v_cvt_pk_bf16_f32 v10, v22, v23
	s_waitcnt vmcnt(8)
	v_cvt_pk_bf16_f32 v13, v32, v33
	v_cvt_pk_bf16_f32 v12, v30, v31
	ds_write2st64_b64 v239, v[10:11], v[12:13] offset0:16 offset1:24
	s_waitcnt vmcnt(7)
	v_cvt_pk_bf16_f32 v11, v36, v37
	v_cvt_pk_bf16_f32 v10, v34, v35
	s_waitcnt vmcnt(6)
	v_cvt_pk_bf16_f32 v13, v40, v41
	v_cvt_pk_bf16_f32 v12, v38, v39
	ds_write2st64_b64 v239, v[10:11], v[12:13] offset0:32 offset1:40
	s_waitcnt vmcnt(5)
	v_cvt_pk_bf16_f32 v11, v44, v45
	v_cvt_pk_bf16_f32 v10, v42, v43
	s_waitcnt vmcnt(4)
	v_cvt_pk_bf16_f32 v13, v48, v49
	v_cvt_pk_bf16_f32 v12, v46, v47
	ds_write2st64_b64 v239, v[10:11], v[12:13] offset0:48 offset1:56
	s_waitcnt lgkmcnt(0)
	s_add_i32 s21, s21, 2
	s_barrier
	s_setprio 1
	s_lshl_b32 s22, s21, 1
	s_and_b32 s22, s22, 0x60
	s_add_i32 s22, s22, s12
	s_lshl_b32 s22, s22, 6
	s_and_b32 s22, s22, 0x3f00
	s_or_b32 s22, s22, s13
	s_lshl_b32 s23, s21, 23
	s_lshl_b32 s22, s22, 9
	s_and_b32 s23, s23, 0x7000000
	s_or_b32 s22, s22, s23
	s_lshl_b32 s23, s21, 8
	s_and_b32 s23, s23, 0x100
	s_or_b32 s22, s22, s23
	s_or_b32 s23, s22, 0x4000
	s_waitcnt lgkmcnt(11)
	v_mfma_f32_16x16x32_bf16 v[174:177], v[178:181], v[206:209], v[240:243]
	v_mfma_f32_16x16x32_bf16 v[170:173], v[194:197], v[206:209], v[244:247]
	v_mfma_f32_16x16x32_bf16 v[158:161], v[198:201], v[206:209], v[248:251]
	buffer_load_dwordx4 v[10:13], v1, s[4:7], s22 offen sc0 nt
	v_mfma_f32_16x16x32_bf16 v[142:145], v[202:205], v[206:209], v[252:255]
	s_waitcnt lgkmcnt(10)
	v_mfma_f32_16x16x32_bf16 v[166:169], v[178:181], v[210:213], v[240:243]
	v_mfma_f32_16x16x32_bf16 v[162:165], v[194:197], v[210:213], v[244:247]
	v_mfma_f32_16x16x32_bf16 v[146:149], v[198:201], v[210:213], v[248:251]
	buffer_load_dwordx4 v[18:21], v1, s[4:7], s23 offen sc0 nt
	s_or_b32 s23, s22, 0x8000
	v_mfma_f32_16x16x32_bf16 v[122:125], v[202:205], v[210:213], v[252:255]
	s_waitcnt lgkmcnt(9)
	v_mfma_f32_16x16x32_bf16 v[154:157], v[178:181], v[214:217], v[240:243]
	v_mfma_f32_16x16x32_bf16 v[150:153], v[194:197], v[214:217], v[244:247]
	v_mfma_f32_16x16x32_bf16 v[130:133], v[198:201], v[214:217], v[248:251]
	buffer_load_dwordx4 v[22:25], v1, s[4:7], s23 offen sc0 nt
	s_or_b32 s23, s22, 0xc000
	v_mfma_f32_16x16x32_bf16 v[106:109], v[202:205], v[214:217], v[252:255]
	s_waitcnt lgkmcnt(8)
	v_mfma_f32_16x16x32_bf16 v[138:141], v[178:181], v[218:221], v[240:243]
	v_mfma_f32_16x16x32_bf16 v[134:137], v[194:197], v[218:221], v[244:247]
	v_mfma_f32_16x16x32_bf16 v[114:117], v[198:201], v[218:221], v[248:251]
	buffer_load_dwordx4 v[30:33], v1, s[4:7], s23 offen sc0 nt
	s_or_b32 s23, s22, 0x10000
	v_mfma_f32_16x16x32_bf16 v[90:93], v[202:205], v[218:221], v[252:255]
	s_waitcnt lgkmcnt(7)
	v_mfma_f32_16x16x32_bf16 v[126:129], v[178:181], v[222:225], v[240:243]
	v_mfma_f32_16x16x32_bf16 v[118:121], v[194:197], v[222:225], v[244:247]
	v_mfma_f32_16x16x32_bf16 v[98:101], v[198:201], v[222:225], v[248:251]
	buffer_load_dwordx4 v[34:37], v1, s[4:7], s23 offen sc0 nt
	s_or_b32 s23, s22, 0x14000
	v_mfma_f32_16x16x32_bf16 v[74:77], v[202:205], v[222:225], v[252:255]
	s_waitcnt lgkmcnt(6)
	v_mfma_f32_16x16x32_bf16 v[110:113], v[178:181], v[226:229], v[240:243]
	v_mfma_f32_16x16x32_bf16 v[102:105], v[194:197], v[226:229], v[244:247]
	v_mfma_f32_16x16x32_bf16 v[82:85], v[198:201], v[226:229], v[248:251]
	buffer_load_dwordx4 v[38:41], v1, s[4:7], s23 offen sc0 nt
	s_or_b32 s23, s22, 0x18000
	s_or_b32 s22, s22, 0x1c000
	v_mfma_f32_16x16x32_bf16 v[62:65], v[202:205], v[226:229], v[252:255]
	s_waitcnt lgkmcnt(5)
	v_mfma_f32_16x16x32_bf16 v[94:97], v[178:181], v[230:233], v[240:243]
	v_mfma_f32_16x16x32_bf16 v[86:89], v[194:197], v[230:233], v[244:247]
	v_mfma_f32_16x16x32_bf16 v[70:73], v[198:201], v[230:233], v[248:251]
	buffer_load_dwordx4 v[42:45], v1, s[4:7], s23 offen sc0 nt
	v_mfma_f32_16x16x32_bf16 v[54:57], v[202:205], v[230:233], v[252:255]
	s_waitcnt lgkmcnt(4)
	v_mfma_f32_16x16x32_bf16 v[78:81], v[178:181], v[234:237], v[240:243]
	v_mfma_f32_16x16x32_bf16 v[66:69], v[194:197], v[234:237], v[244:247]
	v_mfma_f32_16x16x32_bf16 v[58:61], v[198:201], v[234:237], v[248:251]
	buffer_load_dwordx4 v[46:49], v1, s[4:7], s22 offen sc0 nt
	v_mfma_f32_16x16x32_bf16 v[50:53], v[202:205], v[234:237], v[252:255]
	s_setprio 0
	s_waitcnt lgkmcnt(0)
	s_barrier
	ds_read_b128 v[178:181], v182 offset:33792
	ds_read_b128 v[194:197], v182 offset:35840
	ds_read_b128 v[198:201], v182 offset:37888
	ds_read_b128 v[202:205], v182 offset:39936
	ds_read_b128 v[206:209], v238 offset:1024
	ds_read_b128 v[210:213], v238 offset:3072
	ds_read_b128 v[214:217], v238 offset:5120
	ds_read_b128 v[218:221], v238 offset:7168
	ds_read_b128 v[222:225], v238 offset:9216
	ds_read_b128 v[226:229], v238 offset:11264
	ds_read_b128 v[230:233], v238 offset:13312
	ds_read_b128 v[234:237], v238 offset:15360
	v_add_u32_e32 v182, s19, v190
	s_waitcnt vmcnt(11)
	ds_write_b128 v182, v[2:5] offset:32768
	s_waitcnt vmcnt(10)
	ds_write_b128 v182, v[6:9] offset:40960
	s_waitcnt vmcnt(9)
	ds_write_b128 v182, v[14:17] offset:49152
	s_waitcnt vmcnt(8)
	ds_write_b128 v182, v[26:29] offset:57344
	s_waitcnt lgkmcnt(0)
	s_barrier
	s_setprio 1
	s_lshl_b32 s21, s21, 7
	s_and_b32 s21, s21, 0x780
	s_or_b32 s21, s21, s14
	s_or_b32 s22, s21, 0x20000
	s_waitcnt lgkmcnt(11)
	v_mfma_f32_16x16x32_bf16 v[174:177], v[178:181], v[206:209], v[174:177]
	v_mfma_f32_16x16x32_bf16 v[170:173], v[194:197], v[206:209], v[170:173]
	v_mfma_f32_16x16x32_bf16 v[158:161], v[198:201], v[206:209], v[158:161]
	v_mfma_f32_16x16x32_bf16 v[142:145], v[202:205], v[206:209], v[142:145]
	s_waitcnt lgkmcnt(10)
	v_mfma_f32_16x16x32_bf16 v[166:169], v[178:181], v[210:213], v[166:169]
	v_mfma_f32_16x16x32_bf16 v[162:165], v[194:197], v[210:213], v[162:165]
	buffer_load_dwordx4 v[2:5], v188, s[0:3], s21 offen sc1
	v_mfma_f32_16x16x32_bf16 v[146:149], v[198:201], v[210:213], v[146:149]
	v_mfma_f32_16x16x32_bf16 v[122:125], v[202:205], v[210:213], v[122:125]
	s_waitcnt lgkmcnt(9)
	v_mfma_f32_16x16x32_bf16 v[154:157], v[178:181], v[214:217], v[154:157]
	v_mfma_f32_16x16x32_bf16 v[150:153], v[194:197], v[214:217], v[150:153]
	v_mfma_f32_16x16x32_bf16 v[130:133], v[198:201], v[214:217], v[130:133]
	v_mfma_f32_16x16x32_bf16 v[106:109], v[202:205], v[214:217], v[106:109]
	s_waitcnt lgkmcnt(8)
	v_mfma_f32_16x16x32_bf16 v[138:141], v[178:181], v[218:221], v[138:141]
	v_mfma_f32_16x16x32_bf16 v[134:137], v[194:197], v[218:221], v[134:137]
	buffer_load_dwordx4 v[6:9], v188, s[0:3], s22 offen sc1
	s_or_b32 s22, s21, 0x40000
	s_or_b32 s21, s21, 0x60000
	v_mfma_f32_16x16x32_bf16 v[114:117], v[198:201], v[218:221], v[114:117]
	v_mfma_f32_16x16x32_bf16 v[90:93], v[202:205], v[218:221], v[90:93]
	s_waitcnt lgkmcnt(7)
	v_mfma_f32_16x16x32_bf16 v[126:129], v[178:181], v[222:225], v[126:129]
	v_mfma_f32_16x16x32_bf16 v[118:121], v[194:197], v[222:225], v[118:121]
	v_mfma_f32_16x16x32_bf16 v[98:101], v[198:201], v[222:225], v[98:101]
	v_mfma_f32_16x16x32_bf16 v[74:77], v[202:205], v[222:225], v[74:77]
	s_waitcnt lgkmcnt(6)
	v_mfma_f32_16x16x32_bf16 v[110:113], v[178:181], v[226:229], v[110:113]
	v_mfma_f32_16x16x32_bf16 v[102:105], v[194:197], v[226:229], v[102:105]
	buffer_load_dwordx4 v[14:17], v188, s[0:3], s22 offen sc1
	v_mfma_f32_16x16x32_bf16 v[82:85], v[198:201], v[226:229], v[82:85]
	v_mfma_f32_16x16x32_bf16 v[62:65], v[202:205], v[226:229], v[62:65]
	s_waitcnt lgkmcnt(5)
	v_mfma_f32_16x16x32_bf16 v[94:97], v[178:181], v[230:233], v[94:97]
	v_mfma_f32_16x16x32_bf16 v[86:89], v[194:197], v[230:233], v[86:89]
	v_mfma_f32_16x16x32_bf16 v[70:73], v[198:201], v[230:233], v[70:73]
	v_mfma_f32_16x16x32_bf16 v[54:57], v[202:205], v[230:233], v[54:57]
	s_waitcnt lgkmcnt(4)
	v_mfma_f32_16x16x32_bf16 v[78:81], v[178:181], v[234:237], v[78:81]
	v_mfma_f32_16x16x32_bf16 v[66:69], v[194:197], v[234:237], v[66:69]
	buffer_load_dwordx4 v[26:29], v188, s[0:3], s21 offen sc1
	v_mfma_f32_16x16x32_bf16 v[58:61], v[198:201], v[234:237], v[58:61]
	v_mfma_f32_16x16x32_bf16 v[50:53], v[202:205], v[234:237], v[50:53]
	s_setprio 0
	s_branch .LBB1_3
